# P2: SWA V-tile and sink loads issued at unit start ahead of the K staging round trip; GLA prep gate-weight loads no longer wait for the q/k loads
# speedup vs baseline: 1.0815x; 1.0041x over previous
; #define LAS __attribute__((address_space(3)))
; __device__ __forceinline__ void gla_prep_unit(Frame& F, int unit) {
;     const int bh = unit >> 7, n = unit & 127, b = bh >> 3, h = bh & 7, tid = F.tid, lane = F.lane;
;     const bf16_t* PROJ = (const bf16_t*)(F.ws + WS_PROJ);
;     bf16_t* QIN = (bf16_t*)(F.ws + WS_QIN) + (size_t)unit * 64 * 128; bf16_t* KDT = (bf16_t*)(F.ws + WS_KDT) + (size_t)unit * 128 * 64;
;     bf16_t* AM = (bf16_t*)(F.ws + WS_AM) + (size_t)unit * 64 * 64; float* DEC = (float*)(F.ws + WS_DEC) + (size_t)unit * 128;
;     LAS float* gaS = (LAS float*)F.lds; LAS float* tot = gaS + 1024; LAS bf16_t* qinS = (LAS bf16_t*)(F.lds + 8192); LAS bf16_t* kinS = qinS + 64 * GP_ROW;
;     const size_t m0 = (size_t)b * SEQ + 64 * n;
;     const int d = tid & 127, cg = tid >> 7;
;     bf16_t qv[16], kv[16];
; #pragma unroll
;     for (int i = 0; i < 16; ++i) { const bf16_t* pr = PROJ + (m0 + cg * 16 + i) * LDP + h * 128 + d; qv[i] = pr[C_GQ]; kv[i] = pr[C_GK]; }
;     { const int c = tid >> 3, r2 = (tid & 7) * 2; const unsigned w = *(const unsigned*)(PROJ + (m0 + c) * LDP + C_GA + r2); gaS[c * 16 + r2] = bflo(w); gaS[c * 16 + r2 + 1] = bfhi(w); }
;     float w2r[16];
; #pragma unroll
;     for (int r = 0; r < 16; ++r) w2r[r] = F.w2[r * 1024 + h * 128 + d];
;     const float bias = F.gb[h * 128 + d];
.LBB0_264:
	s_ashr_i32 s58, s57, 10
	s_ashr_i32 s59, s58, 31
	s_and_b32 s0, s57, 0x380
	s_lshl_b64 s[58:59], s[58:59], 13
	s_and_b32 s1, s3, 0x1fc0
	s_or_b32 s1, s58, s1
	s_lshl_b32 s28, s0, 1
	v_or_b32_e32 v4, s1, v12
	v_lshl_add_u64 v[2:3], v[14:15], 0, s[28:29]
	v_mad_u64_u32 v[2:3], s[60:61], v4, s43, v[2:3]
	v_or_b32_e32 v6, s1, v168
	v_mov_b64_e32 v[4:5], s[96:97]
	v_mad_u64_u32 v[4:5], s[60:61], v6, s43, v[4:5]
	v_mad_i32_i24 v5, s59, v87, v5
	v_lshl_add_u64 v[4:5], v[4:5], 0, v[8:9]
	v_add_co_u32_e32 v4, vcc, s44, v4
	v_mad_i32_i24 v3, s59, v87, v3
	s_nop 0
	v_addc_co_u32_e32 v5, vcc, 0, v5, vcc
	global_load_dword v5, v[4:5], off offset:1024
	v_add_co_u32_e32 v6, vcc, s44, v2
	s_mov_b32 s1, 0xd000
	s_nop 0
	v_addc_co_u32_e32 v7, vcc, 0, v3, vcc
	v_add_co_u32_e32 v58, vcc, s46, v2
	global_load_ushort v119, v[6:7], off offset:1536
	s_nop 0
	v_addc_co_u32_e32 v59, vcc, 0, v3, vcc
	global_load_ushort v117, v[58:59], off offset:3072
	v_add_co_u32_e32 v58, vcc, s1, v2
	s_mov_b32 s1, 0x9000
	s_nop 0
	v_addc_co_u32_e32 v59, vcc, 0, v3, vcc
	v_add_co_u32_e32 v60, vcc, s1, v2
	s_mov_b32 s1, 0x11000
	s_nop 0
	v_addc_co_u32_e32 v61, vcc, 0, v3, vcc
	global_load_ushort v118, v[58:59], off offset:512
	global_load_ushort v120, v[2:3], off
	global_load_ushort v114, v[60:61], off offset:1024
	global_load_ushort v115, v[2:3], off offset:2048
	global_load_ushort v111, v[6:7], off offset:3584
	global_load_ushort v112, v[58:59], off offset:2560
	v_add_co_u32_e32 v6, vcc, s1, v2
	s_mov_b32 s1, 0x15000
	s_nop 0
	v_addc_co_u32_e32 v7, vcc, 0, v3, vcc
	global_load_ushort v110, v[6:7], off offset:2048
	v_add_co_u32_e32 v6, vcc, s1, v2
	s_mov_b32 s1, 0x1a000
	s_nop 0
	v_addc_co_u32_e32 v7, vcc, 0, v3, vcc
	global_load_ushort v109, v[6:7], off offset:3584
	v_add_co_u32_e32 v6, vcc, s1, v2
	s_mov_b32 s1, 0x1e000
	s_nop 0
	v_addc_co_u32_e32 v7, vcc, 0, v3, vcc
	v_add_co_u32_e32 v58, vcc, s1, v2
	s_mov_b32 s1, 0x12000
	s_nop 0
	v_addc_co_u32_e32 v59, vcc, 0, v3, vcc
	global_load_ushort v107, v[6:7], off offset:1024
	global_load_ushort v104, v[58:59], off offset:2560
	v_add_co_u32_e32 v58, vcc, s1, v2
	s_mov_b32 s1, 0x16000
	s_nop 0
	v_addc_co_u32_e32 v59, vcc, 0, v3, vcc
	global_load_ushort v100, v[58:59], off
	global_load_ushort v101, v[6:7], off offset:3072
	v_add_co_u32_e32 v6, vcc, s1, v2
	s_mov_b32 s1, 0x1f000
	s_nop 0
	v_addc_co_u32_e32 v7, vcc, 0, v3, vcc
	global_load_ushort v102, v[6:7], off offset:1536
	v_add_co_u32_e32 v6, vcc, s1, v2
	s_mov_b32 s1, 0x23000
	s_nop 0
	v_addc_co_u32_e32 v7, vcc, 0, v3, vcc
	global_load_ushort v105, v[6:7], off offset:512
	v_add_co_u32_e32 v6, vcc, s1, v2
	s_mov_b32 s1, 0x27000
	s_nop 0
	v_addc_co_u32_e32 v7, vcc, 0, v3, vcc
	v_add_co_u32_e32 v58, vcc, s1, v2
	s_mov_b32 s1, 0x2b000
	s_nop 0
	v_addc_co_u32_e32 v59, vcc, 0, v3, vcc
	v_add_co_u32_e32 v60, vcc, s1, v2
	s_mov_b32 s1, 0x30000
	s_nop 0
	v_addc_co_u32_e32 v61, vcc, 0, v3, vcc
	global_load_ushort v116, v[6:7], off
	global_load_ushort v113, v[58:59], off offset:1536
	global_load_ushort v108, v[60:61], off offset:3072
	v_add_co_u32_e32 v60, vcc, s1, v2
	s_mov_b32 s1, 0x2c000
	s_nop 0
	v_addc_co_u32_e32 v61, vcc, 0, v3, vcc
	global_load_ushort v106, v[60:61], off offset:512
	global_load_ushort v99, v[6:7], off offset:2048
	v_add_co_u32_e32 v6, vcc, s1, v2
	s_mov_b32 s1, 0x34000
	s_nop 0
	v_addc_co_u32_e32 v7, vcc, 0, v3, vcc
	global_load_ushort v103, v[6:7], off offset:1024
	global_load_ushort v97, v[58:59], off offset:3584
	global_load_ushort v98, v[60:61], off offset:2560
	v_add_co_u32_e32 v6, vcc, s1, v2
	s_mov_b32 s1, 0x38000
	s_nop 0
	v_addc_co_u32_e32 v7, vcc, 0, v3, vcc
	global_load_ushort v96, v[6:7], off offset:2048
	v_add_co_u32_e32 v6, vcc, s1, v2
	s_mov_b32 s1, 0x3d000
	s_nop 0
	v_addc_co_u32_e32 v7, vcc, 0, v3, vcc
	global_load_ushort v95, v[6:7], off offset:3584
	v_add_co_u32_e32 v6, vcc, s1, v2
	s_mov_b32 s1, 0x41000
	s_nop 0
	v_addc_co_u32_e32 v7, vcc, 0, v3, vcc
	v_add_co_u32_e32 v58, vcc, s1, v2
	s_mov_b32 s1, 0x35000
	s_nop 0
	v_addc_co_u32_e32 v59, vcc, 0, v3, vcc
	global_load_ushort v94, v[6:7], off offset:1024
	global_load_ushort v93, v[58:59], off offset:2560
	v_add_co_u32_e32 v58, vcc, s1, v2
	s_mov_b32 s1, 0x39000
	s_nop 0
	v_addc_co_u32_e32 v59, vcc, 0, v3, vcc
	global_load_ushort v91, v[58:59], off
	global_load_ushort v92, v[6:7], off offset:3072
	v_add_co_u32_e32 v6, vcc, s1, v2
	s_mov_b32 s1, 0x42000
	s_nop 0
	v_addc_co_u32_e32 v7, vcc, 0, v3, vcc
	v_add_co_u32_e32 v2, vcc, s1, v2
	v_readlane_b32 s68, v254, 36
	s_nop 0
	v_addc_co_u32_e32 v3, vcc, 0, v3, vcc
	global_load_ushort v89, v[6:7], off offset:1536
	global_load_ushort v90, v[2:3], off offset:512
	v_or_b32_e32 v2, s0, v10
	v_readlane_b32 s69, v254, 37
	v_readlane_b32 s70, v254, 38
	v_readlane_b32 s71, v254, 39
	v_readlane_b32 s72, v254, 40
	v_readlane_b32 s73, v254, 41
	v_readlane_b32 s74, v254, 42
	v_readlane_b32 s75, v254, 43
	v_readlane_b32 s76, v254, 44
	v_readlane_b32 s77, v254, 45
	v_lshlrev_b32_e32 v122, 2, v2
	v_mov_b32_e32 v123, v9
	v_readlane_b32 s78, v254, 46
	v_readlane_b32 s79, v254, 47
	v_readlane_b32 s80, v254, 48
	v_readlane_b32 s81, v254, 49
	v_readlane_b32 s82, v254, 50
	v_readlane_b32 s83, v254, 51
	s_mov_b64 s[68:69], s[76:77]
	s_waitcnt vmcnt(32)
	v_lshlrev_b32_e32 v4, 16, v5
	v_and_b32_e32 v5, 0xffff0000, v5
	v_lshl_add_u64 v[124:125], s[68:69], 0, v[122:123]
	s_movk_i32 s0, 0x2000
	ds_write_b64 v11, v[4:5]
	v_add_co_u32_e32 v4, vcc, s0, v124
	s_movk_i32 s0, 0x6000
	s_nop 0
	v_addc_co_u32_e32 v5, vcc, 0, v125, vcc
	v_add_co_u32_e32 v60, vcc, s44, v124
	global_load_dword v2, v122, s[68:69]
	s_nop 0
	v_addc_co_u32_e32 v61, vcc, 0, v125, vcc
	global_load_dword v6, v[4:5], off offset:-4096
	s_nop 0
	global_load_dword v4, v[4:5], off
	s_nop 0
	global_load_dword v58, v[60:61], off offset:-4096
	global_load_dword v3, v[60:61], off
	v_add_co_u32_e32 v60, vcc, s0, v124
	s_mov_b32 s0, 0xa000
	s_nop 0
	v_addc_co_u32_e32 v61, vcc, 0, v125, vcc
	global_load_dword v7, v[60:61], off offset:-4096
	global_load_dword v5, v[60:61], off
	v_add_co_u32_e32 v60, vcc, s46, v124
	s_mov_b64 s[70:71], s[78:79]
	s_nop 0
	v_addc_co_u32_e32 v61, vcc, 0, v125, vcc
	v_add_co_u32_e32 v62, vcc, s0, v124
	global_load_dword v59, v[60:61], off offset:-4096
	s_nop 0
	global_load_dword v60, v[60:61], off
	v_addc_co_u32_e32 v63, vcc, 0, v125, vcc
	v_add_co_u32_e32 v126, vcc, s47, v124
	global_load_dword v64, v[62:63], off offset:-4096
	s_nop 0
	global_load_dword v62, v[62:63], off
	v_addc_co_u32_e32 v127, vcc, 0, v125, vcc
	global_load_dword v66, v[126:127], off offset:-4096
	global_load_dword v61, v[126:127], off
	v_add_co_u32_e32 v126, vcc, s48, v124
	s_mov_b64 s[72:73], s[80:81]
	s_nop 0
	v_addc_co_u32_e32 v127, vcc, 0, v125, vcc
	v_add_co_u32_e32 v124, vcc, s49, v124
	global_load_dword v65, v[126:127], off offset:-4096
	global_load_dword v63, v[126:127], off
	v_addc_co_u32_e32 v125, vcc, 0, v125, vcc
	global_load_dword v67, v[124:125], off
	global_load_dword v121, v122, s[70:71]
	s_waitcnt lgkmcnt(0)
	s_barrier
; #define LAS __attribute__((address_space(3)))
; __device__ __forceinline__ void gla_prep_unit(Frame& F, int unit) {
;     ...
;     __syncthreads();
;     float bl[16]; float run = 0.f;
; #pragma unroll
;     for (int i = 0; i < 16; ++i) { const int c = cg * 16 + i; float z = bias;
; #pragma unroll
;         for (int r4 = 0; r4 < 4; ++r4) { const f32x4 g4 = *(const LAS f32x4*)(gaS + c * 16 + 4 * r4); z += g4.x * w2r[4 * r4] + g4.y * w2r[4 * r4 + 1] + g4.z * w2r[4 * r4 + 2] + g4.w * w2r[4 * r4 + 3]; }
;         const float ls = fminf(z, 0.f) - __logf(1.0f + __expf(-fabsf(z)));
;         run += ls * (1.f / 16.f); bl[i] = run; }
	ds_read_b128 v[122:125], v13
	ds_read_b128 v[126:129], v13 offset:16
	ds_read_b128 v[132:135], v13 offset:32
	ds_read_b128 v[136:139], v13 offset:48
	s_mov_b64 s[74:75], s[82:83]
	s_waitcnt lgkmcnt(3)
	v_mov_b32_e32 v140, v122
	s_waitcnt lgkmcnt(2)
	v_mov_b32_e32 v141, v126
	v_mov_b32_e32 v126, v123
	s_waitcnt vmcnt(11)
	v_pk_mul_f32 v[122:123], v[6:7], v[126:127]
	s_nop 0
	v_pk_fma_f32 v[122:123], v[2:3], v[140:141], v[122:123]
	v_mov_b32_e32 v126, v124
	v_mov_b32_e32 v127, v128
	s_waitcnt vmcnt(10)
	v_pk_fma_f32 v[122:123], v[4:5], v[126:127], v[122:123]
	v_mov_b32_e32 v128, v125
	s_waitcnt vmcnt(9)
	v_pk_fma_f32 v[122:123], v[58:59], v[128:129], v[122:123]
	s_waitcnt vmcnt(0)
	v_add_f32_e32 v122, v121, v122
	v_add_f32_e32 v126, v122, v123
	s_waitcnt lgkmcnt(0)
	v_mov_b32_e32 v123, v136
	v_mov_b32_e32 v136, v133
	v_mov_b32_e32 v122, v132
	v_pk_mul_f32 v[124:125], v[64:65], v[136:137]
	s_nop 0
	v_pk_fma_f32 v[122:123], v[60:61], v[122:123], v[124:125]
	v_mov_b32_e32 v124, v134
	v_mov_b32_e32 v125, v138
	v_pk_fma_f32 v[122:123], v[62:63], v[124:125], v[122:123]
	v_mov_b32_e32 v138, v135
	v_pk_fma_f32 v[122:123], v[66:67], v[138:139], v[122:123]
	s_nop 0
	v_add_f32_e32 v122, v126, v122
	v_add_f32_e32 v122, v122, v123
	v_min_f32_e32 v123, 0, v122
	v_mul_f32_e64 v122, |v122|, s50
	v_exp_f32_e32 v122, v122
	s_nop 0
	v_add_f32_e32 v122, 1.0, v122
	v_cmp_gt_f32_e32 vcc, s51, v122
	s_nop 1
	v_cndmask_b32_e64 v124, 0, 32, vcc
	v_ldexp_f32 v122, v122, v124
	v_log_f32_e32 v122, v122
	s_nop 0
	v_mul_f32_e32 v124, 0x3f317217, v122
	v_fma_f32 v124, v122, s52, -v124
	v_fmac_f32_e32 v124, 0x3377d1cf, v122
	v_fmac_f32_e32 v124, 0x3f317217, v122
	v_cmp_lt_f32_e64 s[0:1], |v122|, s53
	s_nop 1
	v_cndmask_b32_e64 v122, v122, v124, s[0:1]
	v_cndmask_b32_e32 v124, 0, v88, vcc
	v_sub_f32_e32 v122, v122, v124
	ds_read_b128 v[124:127], v13 offset:64
	ds_read_b128 v[132:135], v13 offset:80
	v_sub_f32_e32 v122, v123, v122
	v_fma_f32 v122, v122, s54, 0
	s_waitcnt lgkmcnt(1)
	v_mov_b32_e32 v128, v124
	s_waitcnt lgkmcnt(0)
	v_mov_b32_e32 v129, v132
	v_mov_b32_e32 v132, v125
	v_pk_mul_f32 v[124:125], v[6:7], v[132:133]
	s_nop 0
	v_pk_fma_f32 v[124:125], v[2:3], v[128:129], v[124:125]
	v_mov_b32_e32 v128, v126
	v_mov_b32_e32 v129, v134
	v_pk_fma_f32 v[124:125], v[4:5], v[128:129], v[124:125]
	v_mov_b32_e32 v134, v127
	v_pk_fma_f32 v[124:125], v[58:59], v[134:135], v[124:125]
	s_nop 0
	v_add_f32_e32 v123, v121, v124
	v_add_f32_e32 v123, v123, v125
	ds_read_b128 v[124:127], v13 offset:96
	ds_read_b128 v[132:135], v13 offset:112
	s_waitcnt lgkmcnt(1)
	v_mov_b32_e32 v128, v124
	s_waitcnt lgkmcnt(0)
	v_mov_b32_e32 v129, v132
	v_mov_b32_e32 v132, v125
	v_pk_mul_f32 v[124:125], v[64:65], v[132:133]
	s_nop 0
	v_pk_fma_f32 v[124:125], v[60:61], v[128:129], v[124:125]
	v_mov_b32_e32 v128, v126
	v_mov_b32_e32 v129, v134
	v_pk_fma_f32 v[124:125], v[62:63], v[128:129], v[124:125]
	v_mov_b32_e32 v134, v127
	v_pk_fma_f32 v[124:125], v[66:67], v[134:135], v[124:125]
	s_nop 0
	v_add_f32_e32 v123, v123, v124
	v_add_f32_e32 v123, v123, v125
	v_min_f32_e32 v124, 0, v123
	v_mul_f32_e64 v123, |v123|, s50
	v_exp_f32_e32 v123, v123
	s_nop 0
	v_add_f32_e32 v123, 1.0, v123
	v_cmp_gt_f32_e32 vcc, s51, v123
	s_nop 1
	v_cndmask_b32_e64 v125, 0, 32, vcc
	v_ldexp_f32 v123, v123, v125
	v_log_f32_e32 v123, v123
	s_nop 0
	v_mul_f32_e32 v125, 0x3f317217, v123
	v_fma_f32 v125, v123, s52, -v125
	v_fmac_f32_e32 v125, 0x3377d1cf, v123
	v_fmac_f32_e32 v125, 0x3f317217, v123
	v_cmp_lt_f32_e64 s[0:1], |v123|, s53
	s_nop 1
	v_cndmask_b32_e64 v123, v123, v125, s[0:1]
	v_cndmask_b32_e32 v125, 0, v88, vcc
	v_sub_f32_e32 v123, v123, v125
	v_sub_f32_e32 v123, v124, v123
	ds_read_b128 v[124:127], v13 offset:128
	ds_read_b128 v[132:135], v13 offset:144
	v_fmamk_f32 v123, v123, 0x3d800000, v122
	s_waitcnt lgkmcnt(1)
	v_mov_b32_e32 v128, v124
	s_waitcnt lgkmcnt(0)
	v_mov_b32_e32 v129, v132
	v_mov_b32_e32 v132, v125
	v_pk_mul_f32 v[124:125], v[6:7], v[132:133]
	s_nop 0
	v_pk_fma_f32 v[124:125], v[2:3], v[128:129], v[124:125]
	v_mov_b32_e32 v128, v126
	v_mov_b32_e32 v129, v134
	v_pk_fma_f32 v[124:125], v[4:5], v[128:129], v[124:125]
	v_mov_b32_e32 v134, v127
	v_pk_fma_f32 v[124:125], v[58:59], v[134:135], v[124:125]
	s_nop 0
	v_add_f32_e32 v124, v121, v124
	v_add_f32_e32 v136, v124, v125
	ds_read_b128 v[124:127], v13 offset:160
	ds_read_b128 v[132:135], v13 offset:176
	s_waitcnt lgkmcnt(1)
	v_mov_b32_e32 v128, v124
	s_waitcnt lgkmcnt(0)
	v_mov_b32_e32 v129, v132
	v_mov_b32_e32 v132, v125
	v_pk_mul_f32 v[124:125], v[64:65], v[132:133]
	s_nop 0
	v_pk_fma_f32 v[124:125], v[60:61], v[128:129], v[124:125]
	v_mov_b32_e32 v128, v126
	v_mov_b32_e32 v129, v134
	v_pk_fma_f32 v[124:125], v[62:63], v[128:129], v[124:125]
	v_mov_b32_e32 v134, v127
	v_pk_fma_f32 v[124:125], v[66:67], v[134:135], v[124:125]
	s_nop 0
	v_add_f32_e32 v124, v136, v124
	v_add_f32_e32 v124, v124, v125
	v_min_f32_e32 v125, 0, v124
	v_mul_f32_e64 v124, |v124|, s50
	v_exp_f32_e32 v124, v124
	s_nop 0
	v_add_f32_e32 v124, 1.0, v124
	v_cmp_gt_f32_e32 vcc, s51, v124
	s_nop 1
	v_cndmask_b32_e64 v126, 0, 32, vcc
	v_ldexp_f32 v124, v124, v126
	v_log_f32_e32 v124, v124
	s_nop 0
	v_mul_f32_e32 v126, 0x3f317217, v124
	v_fma_f32 v126, v124, s52, -v126
	v_fmac_f32_e32 v126, 0x3377d1cf, v124
	v_fmac_f32_e32 v126, 0x3f317217, v124
	v_cmp_lt_f32_e64 s[0:1], |v124|, s53
	s_nop 1
	v_cndmask_b32_e64 v124, v124, v126, s[0:1]
	v_cndmask_b32_e32 v126, 0, v88, vcc
	v_sub_f32_e32 v124, v124, v126
	ds_read_b128 v[126:129], v13 offset:192
	ds_read_b128 v[132:135], v13 offset:208
	v_sub_f32_e32 v124, v125, v124
	v_fmamk_f32 v124, v124, 0x3d800000, v123
	s_waitcnt lgkmcnt(1)
; #define LAS __attribute__((address_space(3)))
; __device__ __forceinline__ void gla_prep_unit(Frame& F, int unit) {
;     ...
;     for (int i = 0; i < 16; ++i) { const int c = cg * 16 + i; float z = bias;
; #pragma unroll
;         for (int r4 = 0; r4 < 4; ++r4) { const f32x4 g4 = *(const LAS f32x4*)(gaS + c * 16 + 4 * r4); z += g4.x * w2r[4 * r4] + g4.y * w2r[4 * r4 + 1] + g4.z * w2r[4 * r4 + 2] + g4.w * w2r[4 * r4 + 3]; }
;         const float ls = fminf(z, 0.f) - __logf(1.0f + __expf(-fabsf(z)));
;         run += ls * (1.f / 16.f); bl[i] = run; }
	v_mov_b32_e32 v136, v126
	s_waitcnt lgkmcnt(0)
	v_mov_b32_e32 v137, v132
	v_mov_b32_e32 v132, v127
	v_pk_mul_f32 v[126:127], v[6:7], v[132:133]
	v_mov_b32_e32 v132, v128
	v_pk_fma_f32 v[126:127], v[2:3], v[136:137], v[126:127]
	v_mov_b32_e32 v133, v134
	v_pk_fma_f32 v[126:127], v[4:5], v[132:133], v[126:127]
	v_mov_b32_e32 v134, v129
	v_pk_fma_f32 v[126:127], v[58:59], v[134:135], v[126:127]
	s_nop 0
	v_add_f32_e32 v125, v121, v126
	v_add_f32_e32 v125, v125, v127
	ds_read_b128 v[126:129], v13 offset:224
	ds_read_b128 v[132:135], v13 offset:240
	s_waitcnt lgkmcnt(1)
	v_mov_b32_e32 v136, v126
	s_waitcnt lgkmcnt(0)
	v_mov_b32_e32 v137, v132
	v_mov_b32_e32 v132, v127
	v_pk_mul_f32 v[126:127], v[64:65], v[132:133]
	v_mov_b32_e32 v132, v128
	v_pk_fma_f32 v[126:127], v[60:61], v[136:137], v[126:127]
	v_mov_b32_e32 v133, v134
	v_pk_fma_f32 v[126:127], v[62:63], v[132:133], v[126:127]
	v_mov_b32_e32 v134, v129
	v_pk_fma_f32 v[126:127], v[66:67], v[134:135], v[126:127]
	s_nop 0
	v_add_f32_e32 v125, v125, v126
	v_add_f32_e32 v125, v125, v127
	v_min_f32_e32 v126, 0, v125
	v_mul_f32_e64 v125, |v125|, s50
	v_exp_f32_e32 v125, v125
	s_nop 0
	v_add_f32_e32 v125, 1.0, v125
	v_cmp_gt_f32_e32 vcc, s51, v125
	s_nop 1
	v_cndmask_b32_e64 v127, 0, 32, vcc
	v_ldexp_f32 v125, v125, v127
	v_log_f32_e32 v125, v125
	s_nop 0
	v_mul_f32_e32 v127, 0x3f317217, v125
	v_fma_f32 v127, v125, s52, -v127
	v_fmac_f32_e32 v127, 0x3377d1cf, v125
	v_fmac_f32_e32 v127, 0x3f317217, v125
	v_cmp_lt_f32_e64 s[0:1], |v125|, s53
	s_nop 1
	v_cndmask_b32_e64 v125, v125, v127, s[0:1]
	v_cndmask_b32_e32 v127, 0, v88, vcc
	v_sub_f32_e32 v125, v125, v127
	v_sub_f32_e32 v125, v126, v125
	ds_read_b128 v[126:129], v13 offset:256
	ds_read_b128 v[132:135], v13 offset:272
	v_fmamk_f32 v125, v125, 0x3d800000, v124
	s_waitcnt lgkmcnt(1)
	v_mov_b32_e32 v136, v126
	s_waitcnt lgkmcnt(0)
	v_mov_b32_e32 v137, v132
	v_mov_b32_e32 v132, v127
	v_pk_mul_f32 v[126:127], v[6:7], v[132:133]
	v_mov_b32_e32 v132, v128
	v_pk_fma_f32 v[126:127], v[2:3], v[136:137], v[126:127]
	v_mov_b32_e32 v133, v134
	v_pk_fma_f32 v[126:127], v[4:5], v[132:133], v[126:127]
	v_mov_b32_e32 v134, v129
	v_pk_fma_f32 v[126:127], v[58:59], v[134:135], v[126:127]
	s_nop 0
	v_add_f32_e32 v126, v121, v126
	v_add_f32_e32 v138, v126, v127
	ds_read_b128 v[126:129], v13 offset:288
	ds_read_b128 v[132:135], v13 offset:304
	s_waitcnt lgkmcnt(1)
	v_mov_b32_e32 v136, v126
	s_waitcnt lgkmcnt(0)
	v_mov_b32_e32 v137, v132
	v_mov_b32_e32 v132, v127
	v_pk_mul_f32 v[126:127], v[64:65], v[132:133]
	v_mov_b32_e32 v132, v128
	v_pk_fma_f32 v[126:127], v[60:61], v[136:137], v[126:127]
	v_mov_b32_e32 v133, v134
	v_pk_fma_f32 v[126:127], v[62:63], v[132:133], v[126:127]
	v_mov_b32_e32 v134, v129
	v_pk_fma_f32 v[126:127], v[66:67], v[134:135], v[126:127]
	s_nop 0
	v_add_f32_e32 v126, v138, v126
	v_add_f32_e32 v126, v126, v127
	v_min_f32_e32 v127, 0, v126
	v_mul_f32_e64 v126, |v126|, s50
	v_exp_f32_e32 v126, v126
	ds_read_b128 v[132:135], v13 offset:320
	ds_read_b128 v[136:139], v13 offset:336
	v_add_f32_e32 v126, 1.0, v126
	v_cmp_gt_f32_e32 vcc, s51, v126
	s_waitcnt lgkmcnt(0)
	v_mov_b32_e32 v129, v136
	v_mov_b32_e32 v136, v133
	v_cndmask_b32_e64 v128, 0, 32, vcc
	v_ldexp_f32 v126, v126, v128
	v_log_f32_e32 v126, v126
	s_nop 0
	v_mul_f32_e32 v128, 0x3f317217, v126
	v_fma_f32 v128, v126, s52, -v128
	v_fmac_f32_e32 v128, 0x3377d1cf, v126
	v_fmac_f32_e32 v128, 0x3f317217, v126
	v_cmp_lt_f32_e64 s[0:1], |v126|, s53
	s_nop 1
	v_cndmask_b32_e64 v126, v126, v128, s[0:1]
	v_cndmask_b32_e32 v128, 0, v88, vcc
	v_sub_f32_e32 v126, v126, v128
	v_mov_b32_e32 v128, v132
	v_pk_mul_f32 v[132:133], v[6:7], v[136:137]
	v_sub_f32_e32 v126, v127, v126
	v_pk_fma_f32 v[128:129], v[2:3], v[128:129], v[132:133]
	v_mov_b32_e32 v132, v134
	v_mov_b32_e32 v133, v138
	v_pk_fma_f32 v[128:129], v[4:5], v[132:133], v[128:129]
	v_mov_b32_e32 v138, v135
	v_pk_fma_f32 v[128:129], v[58:59], v[138:139], v[128:129]
	ds_read_b128 v[132:135], v13 offset:352
	ds_read_b128 v[136:139], v13 offset:368
	v_add_f32_e32 v127, v121, v128
	v_add_f32_e32 v127, v127, v129
	v_fmamk_f32 v126, v126, 0x3d800000, v125
	s_waitcnt lgkmcnt(1)
	v_mov_b32_e32 v128, v132
	s_waitcnt lgkmcnt(0)
	v_mov_b32_e32 v129, v136
	v_mov_b32_e32 v136, v133
	v_pk_mul_f32 v[132:133], v[64:65], v[136:137]
	s_nop 0
	v_pk_fma_f32 v[128:129], v[60:61], v[128:129], v[132:133]
	v_mov_b32_e32 v132, v134
	v_mov_b32_e32 v133, v138
	v_pk_fma_f32 v[128:129], v[62:63], v[132:133], v[128:129]
	v_mov_b32_e32 v138, v135
	v_pk_fma_f32 v[128:129], v[66:67], v[138:139], v[128:129]
	ds_read_b128 v[132:135], v13 offset:384
	ds_read_b128 v[136:139], v13 offset:400
	v_add_f32_e32 v127, v127, v128
	v_add_f32_e32 v127, v127, v129
	v_min_f32_e32 v128, 0, v127
	v_mul_f32_e64 v127, |v127|, s50
	v_exp_f32_e32 v127, v127
	s_nop 0
	v_add_f32_e32 v127, 1.0, v127
	v_cmp_gt_f32_e32 vcc, s51, v127
	s_nop 1
	v_cndmask_b32_e64 v129, 0, 32, vcc
	v_ldexp_f32 v127, v127, v129
	v_log_f32_e32 v127, v127
	s_nop 0
	v_mul_f32_e32 v129, 0x3f317217, v127
	v_fma_f32 v129, v127, s52, -v129
	v_fmac_f32_e32 v129, 0x3377d1cf, v127
	v_fmac_f32_e32 v129, 0x3f317217, v127
	v_cmp_lt_f32_e64 s[0:1], |v127|, s53
	s_nop 1
	v_cndmask_b32_e64 v127, v127, v129, s[0:1]
	v_cndmask_b32_e32 v129, 0, v88, vcc
	v_sub_f32_e32 v127, v127, v129
	s_waitcnt lgkmcnt(0)
	v_mov_b32_e32 v129, v136
	v_mov_b32_e32 v136, v133
	v_sub_f32_e32 v127, v128, v127
	v_mov_b32_e32 v128, v132
	v_pk_mul_f32 v[132:133], v[6:7], v[136:137]
	v_fmamk_f32 v127, v127, 0x3d800000, v126
	v_pk_fma_f32 v[128:129], v[2:3], v[128:129], v[132:133]
	v_mov_b32_e32 v132, v134
	v_mov_b32_e32 v133, v138
	v_pk_fma_f32 v[128:129], v[4:5], v[132:133], v[128:129]
	v_mov_b32_e32 v138, v135
	v_pk_fma_f32 v[128:129], v[58:59], v[138:139], v[128:129]
	ds_read_b128 v[132:135], v13 offset:416
	ds_read_b128 v[136:139], v13 offset:432
	v_add_f32_e32 v128, v121, v128
	v_add_f32_e32 v140, v128, v129
	s_waitcnt lgkmcnt(1)
; #define LAS __attribute__((address_space(3)))
; __device__ __forceinline__ void gla_prep_unit(Frame& F, int unit) {
;     ...
;     for (int i = 0; i < 16; ++i) { const int c = cg * 16 + i; float z = bias;
; #pragma unroll
;         for (int r4 = 0; r4 < 4; ++r4) { const f32x4 g4 = *(const LAS f32x4*)(gaS + c * 16 + 4 * r4); z += g4.x * w2r[4 * r4] + g4.y * w2r[4 * r4 + 1] + g4.z * w2r[4 * r4 + 2] + g4.w * w2r[4 * r4 + 3]; }
;         const float ls = fminf(z, 0.f) - __logf(1.0f + __expf(-fabsf(z)));
;         run += ls * (1.f / 16.f); bl[i] = run; }
	v_mov_b32_e32 v128, v132
	s_waitcnt lgkmcnt(0)
	v_mov_b32_e32 v129, v136
	v_mov_b32_e32 v136, v133
	v_pk_mul_f32 v[132:133], v[64:65], v[136:137]
	s_nop 0
	v_pk_fma_f32 v[128:129], v[60:61], v[128:129], v[132:133]
	v_mov_b32_e32 v132, v134
	v_mov_b32_e32 v133, v138
	v_pk_fma_f32 v[128:129], v[62:63], v[132:133], v[128:129]
	v_mov_b32_e32 v138, v135
	v_pk_fma_f32 v[128:129], v[66:67], v[138:139], v[128:129]
	s_nop 0
	v_add_f32_e32 v128, v140, v128
	v_add_f32_e32 v128, v128, v129
	v_min_f32_e32 v129, 0, v128
	v_mul_f32_e64 v128, |v128|, s50
	v_exp_f32_e32 v128, v128
	s_nop 0
	v_add_f32_e32 v128, 1.0, v128
	v_cmp_gt_f32_e32 vcc, s51, v128
	s_nop 1
	v_cndmask_b32_e64 v132, 0, 32, vcc
	v_ldexp_f32 v128, v128, v132
	v_log_f32_e32 v128, v128
	s_nop 0
	v_mul_f32_e32 v132, 0x3f317217, v128
	v_fma_f32 v132, v128, s52, -v132
	v_fmac_f32_e32 v132, 0x3377d1cf, v128
	v_fmac_f32_e32 v132, 0x3f317217, v128
	v_cmp_lt_f32_e64 s[0:1], |v128|, s53
	s_nop 1
	v_cndmask_b32_e64 v128, v128, v132, s[0:1]
	v_cndmask_b32_e32 v132, 0, v88, vcc
	v_sub_f32_e32 v128, v128, v132
	ds_read_b128 v[132:135], v13 offset:448
	ds_read_b128 v[136:139], v13 offset:464
	v_sub_f32_e32 v128, v129, v128
	v_fmamk_f32 v128, v128, 0x3d800000, v127
	s_waitcnt lgkmcnt(1)
	v_mov_b32_e32 v140, v132
	s_waitcnt lgkmcnt(0)
	v_mov_b32_e32 v141, v136
	v_mov_b32_e32 v136, v133
	v_pk_mul_f32 v[132:133], v[6:7], v[136:137]
	v_mov_b32_e32 v136, v134
	v_pk_fma_f32 v[132:133], v[2:3], v[140:141], v[132:133]
	v_mov_b32_e32 v137, v138
	v_pk_fma_f32 v[132:133], v[4:5], v[136:137], v[132:133]
	v_mov_b32_e32 v138, v135
	v_pk_fma_f32 v[132:133], v[58:59], v[138:139], v[132:133]
	s_nop 0
	v_add_f32_e32 v129, v121, v132
	v_add_f32_e32 v129, v129, v133
	ds_read_b128 v[132:135], v13 offset:480
	ds_read_b128 v[136:139], v13 offset:496
	s_waitcnt lgkmcnt(1)
	v_mov_b32_e32 v140, v132
	s_waitcnt lgkmcnt(0)
	v_mov_b32_e32 v141, v136
	v_mov_b32_e32 v136, v133
	v_pk_mul_f32 v[132:133], v[64:65], v[136:137]
	v_mov_b32_e32 v136, v134
	v_pk_fma_f32 v[132:133], v[60:61], v[140:141], v[132:133]
	v_mov_b32_e32 v137, v138
	v_pk_fma_f32 v[132:133], v[62:63], v[136:137], v[132:133]
	v_mov_b32_e32 v138, v135
	v_pk_fma_f32 v[132:133], v[66:67], v[138:139], v[132:133]
	s_nop 0
	v_add_f32_e32 v129, v129, v132
	v_add_f32_e32 v129, v129, v133
	v_min_f32_e32 v132, 0, v129
	v_mul_f32_e64 v129, |v129|, s50
	v_exp_f32_e32 v129, v129
	s_nop 0
	v_add_f32_e32 v129, 1.0, v129
	v_cmp_gt_f32_e32 vcc, s51, v129
	s_nop 1
	v_cndmask_b32_e64 v133, 0, 32, vcc
	v_ldexp_f32 v129, v129, v133
	v_log_f32_e32 v129, v129
	s_nop 0
	v_mul_f32_e32 v133, 0x3f317217, v129
	v_fma_f32 v133, v129, s52, -v133
	v_fmac_f32_e32 v133, 0x3377d1cf, v129
	v_fmac_f32_e32 v133, 0x3f317217, v129
	v_cmp_lt_f32_e64 s[0:1], |v129|, s53
	s_nop 1
	v_cndmask_b32_e64 v129, v129, v133, s[0:1]
	v_cndmask_b32_e32 v133, 0, v88, vcc
	v_sub_f32_e32 v129, v129, v133
	v_sub_f32_e32 v129, v132, v129
	ds_read_b128 v[132:135], v13 offset:512
	ds_read_b128 v[136:139], v13 offset:528
	v_fmamk_f32 v129, v129, 0x3d800000, v128
	s_waitcnt lgkmcnt(1)
	v_mov_b32_e32 v140, v132
	s_waitcnt lgkmcnt(0)
	v_mov_b32_e32 v141, v136
	v_mov_b32_e32 v136, v133
	v_pk_mul_f32 v[132:133], v[6:7], v[136:137]
	v_mov_b32_e32 v136, v134
	v_pk_fma_f32 v[132:133], v[2:3], v[140:141], v[132:133]
	v_mov_b32_e32 v137, v138
	v_pk_fma_f32 v[132:133], v[4:5], v[136:137], v[132:133]
	v_mov_b32_e32 v138, v135
	v_pk_fma_f32 v[132:133], v[58:59], v[138:139], v[132:133]
	s_nop 0
	v_add_f32_e32 v132, v121, v132
	v_add_f32_e32 v142, v132, v133
	ds_read_b128 v[132:135], v13 offset:544
	ds_read_b128 v[136:139], v13 offset:560
	s_waitcnt lgkmcnt(1)
	v_mov_b32_e32 v140, v132
	s_waitcnt lgkmcnt(0)
	v_mov_b32_e32 v141, v136
	v_mov_b32_e32 v136, v133
	v_pk_mul_f32 v[132:133], v[64:65], v[136:137]
	v_mov_b32_e32 v136, v134
	v_pk_fma_f32 v[132:133], v[60:61], v[140:141], v[132:133]
	v_mov_b32_e32 v137, v138
	v_pk_fma_f32 v[132:133], v[62:63], v[136:137], v[132:133]
	v_mov_b32_e32 v138, v135
	v_pk_fma_f32 v[132:133], v[66:67], v[138:139], v[132:133]
	s_nop 0
	v_add_f32_e32 v132, v142, v132
	v_add_f32_e32 v132, v132, v133
	v_min_f32_e32 v133, 0, v132
	v_mul_f32_e64 v132, |v132|, s50
	v_exp_f32_e32 v132, v132
	s_nop 0
	v_add_f32_e32 v132, 1.0, v132
	v_cmp_gt_f32_e32 vcc, s51, v132
	s_nop 1
	v_cndmask_b32_e64 v134, 0, 32, vcc
	v_ldexp_f32 v132, v132, v134
	v_log_f32_e32 v132, v132
	s_nop 0
	v_mul_f32_e32 v134, 0x3f317217, v132
	v_fma_f32 v134, v132, s52, -v134
	v_fmac_f32_e32 v134, 0x3377d1cf, v132
	v_fmac_f32_e32 v134, 0x3f317217, v132
	v_cmp_lt_f32_e64 s[0:1], |v132|, s53
	s_nop 1
	v_cndmask_b32_e64 v132, v132, v134, s[0:1]
	v_cndmask_b32_e32 v134, 0, v88, vcc
	v_sub_f32_e32 v132, v132, v134
	ds_read_b128 v[134:137], v13 offset:576
	ds_read_b128 v[138:141], v13 offset:592
	v_sub_f32_e32 v132, v133, v132
	v_fmamk_f32 v132, v132, 0x3d800000, v129
	s_waitcnt lgkmcnt(1)
	v_mov_b32_e32 v142, v134
	s_waitcnt lgkmcnt(0)
	v_mov_b32_e32 v143, v138
	v_mov_b32_e32 v138, v135
	v_pk_mul_f32 v[134:135], v[6:7], v[138:139]
	v_mov_b32_e32 v138, v136
	v_pk_fma_f32 v[134:135], v[2:3], v[142:143], v[134:135]
	v_mov_b32_e32 v139, v140
	v_pk_fma_f32 v[134:135], v[4:5], v[138:139], v[134:135]
	v_mov_b32_e32 v140, v137
	v_pk_fma_f32 v[134:135], v[58:59], v[140:141], v[134:135]
	s_nop 0
	v_add_f32_e32 v133, v121, v134
	v_add_f32_e32 v133, v133, v135
	ds_read_b128 v[134:137], v13 offset:608
	ds_read_b128 v[138:141], v13 offset:624
	s_waitcnt lgkmcnt(1)
	v_mov_b32_e32 v142, v134
	s_waitcnt lgkmcnt(0)
; #define LAS __attribute__((address_space(3)))
; __device__ __forceinline__ void gla_prep_unit(Frame& F, int unit) {
;     ...
;     for (int i = 0; i < 16; ++i) { const int c = cg * 16 + i; float z = bias;
; #pragma unroll
;         for (int r4 = 0; r4 < 4; ++r4) { const f32x4 g4 = *(const LAS f32x4*)(gaS + c * 16 + 4 * r4); z += g4.x * w2r[4 * r4] + g4.y * w2r[4 * r4 + 1] + g4.z * w2r[4 * r4 + 2] + g4.w * w2r[4 * r4 + 3]; }
;         const float ls = fminf(z, 0.f) - __logf(1.0f + __expf(-fabsf(z)));
;         run += ls * (1.f / 16.f); bl[i] = run; }
	v_mov_b32_e32 v143, v138
	v_mov_b32_e32 v138, v135
	v_pk_mul_f32 v[134:135], v[64:65], v[138:139]
	v_mov_b32_e32 v138, v136
	v_pk_fma_f32 v[134:135], v[60:61], v[142:143], v[134:135]
	v_mov_b32_e32 v139, v140
	v_pk_fma_f32 v[134:135], v[62:63], v[138:139], v[134:135]
	v_mov_b32_e32 v140, v137
	v_pk_fma_f32 v[134:135], v[66:67], v[140:141], v[134:135]
	s_nop 0
	v_add_f32_e32 v133, v133, v134
	v_add_f32_e32 v133, v133, v135
	v_min_f32_e32 v134, 0, v133
	v_mul_f32_e64 v133, |v133|, s50
	v_exp_f32_e32 v133, v133
	s_nop 0
	v_add_f32_e32 v133, 1.0, v133
	v_cmp_gt_f32_e32 vcc, s51, v133
	s_nop 1
	v_cndmask_b32_e64 v135, 0, 32, vcc
	v_ldexp_f32 v133, v133, v135
	v_log_f32_e32 v133, v133
	s_nop 0
	v_mul_f32_e32 v135, 0x3f317217, v133
	v_fma_f32 v135, v133, s52, -v135
	v_fmac_f32_e32 v135, 0x3377d1cf, v133
	v_fmac_f32_e32 v135, 0x3f317217, v133
	v_cmp_lt_f32_e64 s[0:1], |v133|, s53
	s_nop 1
	v_cndmask_b32_e64 v133, v133, v135, s[0:1]
	v_cndmask_b32_e32 v135, 0, v88, vcc
	v_sub_f32_e32 v133, v133, v135
	v_sub_f32_e32 v133, v134, v133
	ds_read_b128 v[134:137], v13 offset:640
	ds_read_b128 v[138:141], v13 offset:656
	v_fmamk_f32 v133, v133, 0x3d800000, v132
	s_waitcnt lgkmcnt(1)
	v_mov_b32_e32 v142, v134
	s_waitcnt lgkmcnt(0)
	v_mov_b32_e32 v143, v138
	v_mov_b32_e32 v138, v135
	v_pk_mul_f32 v[134:135], v[6:7], v[138:139]
	v_mov_b32_e32 v138, v136
	v_pk_fma_f32 v[134:135], v[2:3], v[142:143], v[134:135]
	v_mov_b32_e32 v139, v140
	v_pk_fma_f32 v[134:135], v[4:5], v[138:139], v[134:135]
	v_mov_b32_e32 v140, v137
	v_pk_fma_f32 v[134:135], v[58:59], v[140:141], v[134:135]
	s_nop 0
	v_add_f32_e32 v134, v121, v134
	v_add_f32_e32 v144, v134, v135
	ds_read_b128 v[134:137], v13 offset:672
	ds_read_b128 v[138:141], v13 offset:688
	s_waitcnt lgkmcnt(1)
	v_mov_b32_e32 v142, v134
	s_waitcnt lgkmcnt(0)
	v_mov_b32_e32 v143, v138
	v_mov_b32_e32 v138, v135
	v_pk_mul_f32 v[134:135], v[64:65], v[138:139]
	v_mov_b32_e32 v138, v136
	v_pk_fma_f32 v[134:135], v[60:61], v[142:143], v[134:135]
	v_mov_b32_e32 v139, v140
	v_pk_fma_f32 v[134:135], v[62:63], v[138:139], v[134:135]
	v_mov_b32_e32 v140, v137
	v_pk_fma_f32 v[134:135], v[66:67], v[140:141], v[134:135]
	s_nop 0
	v_add_f32_e32 v134, v144, v134
	v_add_f32_e32 v134, v134, v135
	v_min_f32_e32 v135, 0, v134
	v_mul_f32_e64 v134, |v134|, s50
	v_exp_f32_e32 v134, v134
	s_nop 0
	v_add_f32_e32 v134, 1.0, v134
	v_cmp_gt_f32_e32 vcc, s51, v134
	s_nop 1
	v_cndmask_b32_e64 v136, 0, 32, vcc
	v_ldexp_f32 v134, v134, v136
	v_log_f32_e32 v134, v134
	s_nop 0
	v_mul_f32_e32 v136, 0x3f317217, v134
	v_fma_f32 v136, v134, s52, -v136
	v_fmac_f32_e32 v136, 0x3377d1cf, v134
	v_fmac_f32_e32 v136, 0x3f317217, v134
	v_cmp_lt_f32_e64 s[0:1], |v134|, s53
	s_nop 1
	v_cndmask_b32_e64 v134, v134, v136, s[0:1]
	v_cndmask_b32_e32 v136, 0, v88, vcc
	v_sub_f32_e32 v134, v134, v136
	ds_read_b128 v[136:139], v13 offset:704
	ds_read_b128 v[140:143], v13 offset:720
	v_sub_f32_e32 v134, v135, v134
	v_fmamk_f32 v134, v134, 0x3d800000, v133
	s_waitcnt lgkmcnt(1)
	v_mov_b32_e32 v144, v136
	s_waitcnt lgkmcnt(0)
	v_mov_b32_e32 v145, v140
	v_mov_b32_e32 v140, v137
	v_pk_mul_f32 v[136:137], v[6:7], v[140:141]
	v_mov_b32_e32 v140, v138
	v_pk_fma_f32 v[136:137], v[2:3], v[144:145], v[136:137]
	v_mov_b32_e32 v141, v142
	v_pk_fma_f32 v[136:137], v[4:5], v[140:141], v[136:137]
	v_mov_b32_e32 v142, v139
	v_pk_fma_f32 v[136:137], v[58:59], v[142:143], v[136:137]
	s_nop 0
	v_add_f32_e32 v135, v121, v136
	v_add_f32_e32 v135, v135, v137
	ds_read_b128 v[136:139], v13 offset:736
	ds_read_b128 v[140:143], v13 offset:752
	s_waitcnt lgkmcnt(1)
	v_mov_b32_e32 v144, v136
	s_waitcnt lgkmcnt(0)
	v_mov_b32_e32 v145, v140
	v_mov_b32_e32 v140, v137
	v_pk_mul_f32 v[136:137], v[64:65], v[140:141]
	v_mov_b32_e32 v140, v138
	v_pk_fma_f32 v[136:137], v[60:61], v[144:145], v[136:137]
	v_mov_b32_e32 v141, v142
	v_pk_fma_f32 v[136:137], v[62:63], v[140:141], v[136:137]
	v_mov_b32_e32 v142, v139
	v_pk_fma_f32 v[136:137], v[66:67], v[142:143], v[136:137]
	s_nop 0
	v_add_f32_e32 v135, v135, v136
	v_add_f32_e32 v135, v135, v137
	v_min_f32_e32 v136, 0, v135
	v_mul_f32_e64 v135, |v135|, s50
	v_exp_f32_e32 v135, v135
	s_nop 0
	v_add_f32_e32 v135, 1.0, v135
	v_cmp_gt_f32_e32 vcc, s51, v135
	s_nop 1
	v_cndmask_b32_e64 v137, 0, 32, vcc
	v_ldexp_f32 v135, v135, v137
	v_log_f32_e32 v135, v135
	s_nop 0
	v_mul_f32_e32 v137, 0x3f317217, v135
	v_fma_f32 v137, v135, s52, -v137
	v_fmac_f32_e32 v137, 0x3377d1cf, v135
	v_fmac_f32_e32 v137, 0x3f317217, v135
	v_cmp_lt_f32_e64 s[0:1], |v135|, s53
	s_nop 1
	v_cndmask_b32_e64 v135, v135, v137, s[0:1]
	v_cndmask_b32_e32 v137, 0, v88, vcc
	v_sub_f32_e32 v135, v135, v137
	v_sub_f32_e32 v135, v136, v135
	ds_read_b128 v[136:139], v13 offset:768
	ds_read_b128 v[140:143], v13 offset:784
	v_fmamk_f32 v135, v135, 0x3d800000, v134
	s_waitcnt lgkmcnt(1)
	v_mov_b32_e32 v144, v136
	s_waitcnt lgkmcnt(0)
	v_mov_b32_e32 v145, v140
	v_mov_b32_e32 v140, v137
	v_pk_mul_f32 v[136:137], v[6:7], v[140:141]
	v_mov_b32_e32 v140, v138
	v_pk_fma_f32 v[136:137], v[2:3], v[144:145], v[136:137]
	v_mov_b32_e32 v141, v142
	v_pk_fma_f32 v[136:137], v[4:5], v[140:141], v[136:137]
	v_mov_b32_e32 v142, v139
	v_pk_fma_f32 v[136:137], v[58:59], v[142:143], v[136:137]
	s_nop 0
	v_add_f32_e32 v136, v121, v136
	v_add_f32_e32 v146, v136, v137
	ds_read_b128 v[136:139], v13 offset:800
	ds_read_b128 v[140:143], v13 offset:816
	s_waitcnt lgkmcnt(1)
	v_mov_b32_e32 v144, v136
	s_waitcnt lgkmcnt(0)
; #define LAS __attribute__((address_space(3)))
; __device__ __forceinline__ void gla_prep_unit(Frame& F, int unit) {
;     ...
;     for (int i = 0; i < 16; ++i) { const int c = cg * 16 + i; float z = bias;
; #pragma unroll
;         for (int r4 = 0; r4 < 4; ++r4) { const f32x4 g4 = *(const LAS f32x4*)(gaS + c * 16 + 4 * r4); z += g4.x * w2r[4 * r4] + g4.y * w2r[4 * r4 + 1] + g4.z * w2r[4 * r4 + 2] + g4.w * w2r[4 * r4 + 3]; }
;         const float ls = fminf(z, 0.f) - __logf(1.0f + __expf(-fabsf(z)));
;         run += ls * (1.f / 16.f); bl[i] = run; }
;     tot[cg * 128 + d] = run;
;     __syncthreads();
	v_mov_b32_e32 v145, v140
	v_mov_b32_e32 v140, v137
	v_pk_mul_f32 v[136:137], v[64:65], v[140:141]
	v_mov_b32_e32 v140, v138
	v_pk_fma_f32 v[136:137], v[60:61], v[144:145], v[136:137]
	v_mov_b32_e32 v141, v142
	v_pk_fma_f32 v[136:137], v[62:63], v[140:141], v[136:137]
	v_mov_b32_e32 v142, v139
	v_pk_fma_f32 v[136:137], v[66:67], v[142:143], v[136:137]
	s_nop 0
	v_add_f32_e32 v136, v146, v136
	v_add_f32_e32 v136, v136, v137
	v_min_f32_e32 v137, 0, v136
	v_mul_f32_e64 v136, |v136|, s50
	v_exp_f32_e32 v136, v136
	s_nop 0
	v_add_f32_e32 v136, 1.0, v136
	v_cmp_gt_f32_e32 vcc, s51, v136
	s_nop 1
	v_cndmask_b32_e64 v138, 0, 32, vcc
	v_ldexp_f32 v136, v136, v138
	v_log_f32_e32 v136, v136
	s_nop 0
	v_mul_f32_e32 v138, 0x3f317217, v136
	v_fma_f32 v138, v136, s52, -v138
	v_fmac_f32_e32 v138, 0x3377d1cf, v136
	v_fmac_f32_e32 v138, 0x3f317217, v136
	v_cmp_lt_f32_e64 s[0:1], |v136|, s53
	s_nop 1
	v_cndmask_b32_e64 v136, v136, v138, s[0:1]
	v_cndmask_b32_e32 v138, 0, v88, vcc
	v_sub_f32_e32 v136, v136, v138
	ds_read_b128 v[138:141], v13 offset:832
	ds_read_b128 v[142:145], v13 offset:848
	v_sub_f32_e32 v136, v137, v136
	v_fmamk_f32 v136, v136, 0x3d800000, v135
	s_waitcnt lgkmcnt(1)
	v_mov_b32_e32 v146, v138
	s_waitcnt lgkmcnt(0)
	v_mov_b32_e32 v147, v142
	v_mov_b32_e32 v142, v139
	v_pk_mul_f32 v[138:139], v[6:7], v[142:143]
	v_mov_b32_e32 v142, v140
	v_pk_fma_f32 v[138:139], v[2:3], v[146:147], v[138:139]
	v_mov_b32_e32 v143, v144
	v_pk_fma_f32 v[138:139], v[4:5], v[142:143], v[138:139]
	v_mov_b32_e32 v144, v141
	v_pk_fma_f32 v[138:139], v[58:59], v[144:145], v[138:139]
	s_nop 0
	v_add_f32_e32 v137, v121, v138
	v_add_f32_e32 v137, v137, v139
	ds_read_b128 v[138:141], v13 offset:864
	ds_read_b128 v[142:145], v13 offset:880
	s_waitcnt lgkmcnt(1)
	v_mov_b32_e32 v146, v138
	s_waitcnt lgkmcnt(0)
	v_mov_b32_e32 v147, v142
	v_mov_b32_e32 v142, v139
	v_pk_mul_f32 v[138:139], v[64:65], v[142:143]
	v_mov_b32_e32 v142, v140
	v_pk_fma_f32 v[138:139], v[60:61], v[146:147], v[138:139]
	v_mov_b32_e32 v143, v144
	v_pk_fma_f32 v[138:139], v[62:63], v[142:143], v[138:139]
	v_mov_b32_e32 v144, v141
	v_pk_fma_f32 v[138:139], v[66:67], v[144:145], v[138:139]
	s_nop 0
	v_add_f32_e32 v137, v137, v138
	v_add_f32_e32 v137, v137, v139
	v_min_f32_e32 v138, 0, v137
	v_mul_f32_e64 v137, |v137|, s50
	v_exp_f32_e32 v137, v137
	s_nop 0
	v_add_f32_e32 v137, 1.0, v137
	v_cmp_gt_f32_e32 vcc, s51, v137
	s_nop 1
	v_cndmask_b32_e64 v139, 0, 32, vcc
	v_ldexp_f32 v137, v137, v139
	v_log_f32_e32 v137, v137
	s_nop 0
	v_mul_f32_e32 v139, 0x3f317217, v137
	v_fma_f32 v139, v137, s52, -v139
	v_fmac_f32_e32 v139, 0x3377d1cf, v137
	v_fmac_f32_e32 v139, 0x3f317217, v137
	v_cmp_lt_f32_e64 s[0:1], |v137|, s53
	s_nop 1
	v_cndmask_b32_e64 v137, v137, v139, s[0:1]
	v_cndmask_b32_e32 v139, 0, v88, vcc
	v_sub_f32_e32 v137, v137, v139
	v_sub_f32_e32 v137, v138, v137
	ds_read_b128 v[138:141], v13 offset:896
	ds_read_b128 v[142:145], v13 offset:912
	v_fmamk_f32 v137, v137, 0x3d800000, v136
	s_waitcnt lgkmcnt(1)
	v_mov_b32_e32 v146, v138
	s_waitcnt lgkmcnt(0)
	v_mov_b32_e32 v147, v142
	v_mov_b32_e32 v142, v139
	v_pk_mul_f32 v[138:139], v[6:7], v[142:143]
	v_mov_b32_e32 v142, v140
	v_pk_fma_f32 v[138:139], v[2:3], v[146:147], v[138:139]
	v_mov_b32_e32 v143, v144
	v_pk_fma_f32 v[138:139], v[4:5], v[142:143], v[138:139]
	v_mov_b32_e32 v144, v141
	v_pk_fma_f32 v[138:139], v[58:59], v[144:145], v[138:139]
	s_nop 0
	v_add_f32_e32 v138, v121, v138
	v_add_f32_e32 v148, v138, v139
	ds_read_b128 v[138:141], v13 offset:928
	ds_read_b128 v[142:145], v13 offset:944
	s_waitcnt lgkmcnt(1)
	v_mov_b32_e32 v146, v138
	s_waitcnt lgkmcnt(0)
	v_mov_b32_e32 v147, v142
	v_mov_b32_e32 v142, v139
	v_pk_mul_f32 v[138:139], v[64:65], v[142:143]
	v_mov_b32_e32 v142, v140
	v_pk_fma_f32 v[138:139], v[60:61], v[146:147], v[138:139]
	v_mov_b32_e32 v143, v144
	v_pk_fma_f32 v[138:139], v[62:63], v[142:143], v[138:139]
	v_mov_b32_e32 v144, v141
	v_pk_fma_f32 v[138:139], v[66:67], v[144:145], v[138:139]
	s_nop 0
	v_add_f32_e32 v138, v148, v138
	v_add_f32_e32 v138, v138, v139
	v_min_f32_e32 v139, 0, v138
	v_mul_f32_e64 v138, |v138|, s50
	v_exp_f32_e32 v138, v138
	s_nop 0
	v_add_f32_e32 v138, 1.0, v138
	v_cmp_gt_f32_e32 vcc, s51, v138
	s_nop 1
	v_cndmask_b32_e64 v140, 0, 32, vcc
	v_ldexp_f32 v138, v138, v140
	v_log_f32_e32 v138, v138
	s_nop 0
	v_mul_f32_e32 v140, 0x3f317217, v138
	v_fma_f32 v140, v138, s52, -v140
	v_fmac_f32_e32 v140, 0x3377d1cf, v138
	v_fmac_f32_e32 v140, 0x3f317217, v138
	v_cmp_lt_f32_e64 s[0:1], |v138|, s53
	s_nop 1
	v_cndmask_b32_e64 v138, v138, v140, s[0:1]
	v_cndmask_b32_e32 v140, 0, v88, vcc
	v_sub_f32_e32 v138, v138, v140
	ds_read_b128 v[140:143], v13 offset:960
	ds_read_b128 v[144:147], v13 offset:976
	v_sub_f32_e32 v138, v139, v138
	v_fmamk_f32 v138, v138, 0x3d800000, v137
	s_waitcnt lgkmcnt(1)
	v_mov_b32_e32 v148, v140
	s_waitcnt lgkmcnt(0)
	v_mov_b32_e32 v149, v144
	v_mov_b32_e32 v144, v141
	v_pk_mul_f32 v[6:7], v[6:7], v[144:145]
	s_nop 0
	v_pk_fma_f32 v[2:3], v[2:3], v[148:149], v[6:7]
	v_mov_b32_e32 v6, v142
	v_mov_b32_e32 v7, v146
	v_pk_fma_f32 v[2:3], v[4:5], v[6:7], v[2:3]
	v_mov_b32_e32 v146, v143
	v_pk_fma_f32 v[2:3], v[58:59], v[146:147], v[2:3]
	s_nop 0
	v_add_f32_e32 v2, v121, v2
	v_add_f32_e32 v58, v2, v3
	ds_read_b128 v[2:5], v13 offset:992
	ds_read_b128 v[140:143], v13 offset:1008
	s_waitcnt lgkmcnt(1)
	v_mov_b32_e32 v6, v2
	s_waitcnt lgkmcnt(0)
	v_mov_b32_e32 v7, v140
	v_mov_b32_e32 v140, v3
	v_pk_mul_f32 v[2:3], v[64:65], v[140:141]
	s_nop 0
	v_pk_fma_f32 v[2:3], v[60:61], v[6:7], v[2:3]
	v_mov_b32_e32 v6, v4
	v_mov_b32_e32 v7, v142
	v_pk_fma_f32 v[2:3], v[62:63], v[6:7], v[2:3]
	v_mov_b32_e32 v142, v5
	v_pk_fma_f32 v[2:3], v[66:67], v[142:143], v[2:3]
	s_nop 0
	v_add_f32_e32 v2, v58, v2
	v_add_f32_e32 v2, v2, v3
	v_min_f32_e32 v3, 0, v2
	v_mul_f32_e64 v2, |v2|, s50
	v_exp_f32_e32 v2, v2
	v_lshl_add_u64 v[58:59], s[66:67], 0, v[28:29]
	v_add_f32_e32 v2, 1.0, v2
	v_cmp_gt_f32_e32 vcc, s51, v2
	s_nop 1
	v_cndmask_b32_e64 v4, 0, 32, vcc
	v_ldexp_f32 v2, v2, v4
	v_log_f32_e32 v2, v2
	s_nop 0
	v_mul_f32_e32 v4, 0x3f317217, v2
	v_fma_f32 v4, v2, s52, -v4
	v_fmac_f32_e32 v4, 0x3377d1cf, v2
	v_fmac_f32_e32 v4, 0x3f317217, v2
	v_cmp_lt_f32_e64 s[0:1], |v2|, s53
	s_nop 1
	v_cndmask_b32_e64 v2, v2, v4, s[0:1]
	v_cndmask_b32_e32 v4, 0, v88, vcc
	v_sub_f32_e32 v2, v2, v4
	v_sub_f32_e32 v2, v3, v2
	v_fmamk_f32 v3, v2, 0x3d800000, v138
	ds_write_b32 v68, v3 offset:4096
	s_waitcnt lgkmcnt(0)
	s_barrier
; __device__ __forceinline__ unsigned f2bf(float f) { unsigned u = __builtin_bit_cast(unsigned, f); return (u + 0x7fffu + ((u >> 16) & 1u)) >> 16; }
; __device__ __forceinline__ void gla_prep_unit(Frame& F, int unit) {
;     ...
;     float offs = 0.f, blast = 0.f;
; #pragma unroll
;     for (int g = 0; g < 4; ++g) { const float t = tot[g * 128 + d]; blast += t; if (g < cg) offs += t; }
;     const float eblast = __expf(blast);
;     unsigned kd[8];
; #pragma unroll
;     for (int i = 0; i < 16; i += 2) { float kdv[2];
; #pragma unroll
;         for (int u = 0; u < 2; ++u) { const int c = cg * 16 + i + u; const float bb = bl[i + u] + offs;
;             const float q = bf2f(qv[i + u]) * 0.08838834764831845f, k = bf2f(kv[i + u]);
;             const float eb = __expf(bb), einv = __builtin_amdgcn_rcpf(eb);
;             const float qin = q * eb, kin = k * einv; kdv[u] = kin * eblast;
;             const bf16_t qb16 = (bf16_t)f2bf(qin); qinS[c * GP_ROW + d] = qb16; kinS[c * GP_ROW + d] = (bf16_t)f2bf(kin); QIN[c * 128 + d] = qb16; }
	ds_read2st64_b32 v[4:5], v69 offset0:16 offset1:18
	s_waitcnt lgkmcnt(0)
	v_add_f32_e32 v2, 0, v4
	v_cndmask_b32_e64 v4, v2, 0, s[4:5]
	v_add_f32_e32 v2, v2, v5
	v_add_f32_e32 v5, v5, v4
	v_cndmask_b32_e64 v6, v4, v5, s[6:7]
	ds_read2st64_b32 v[4:5], v69 offset0:20 offset1:22
	s_waitcnt lgkmcnt(0)
	v_add_f32_e32 v2, v2, v4
	v_add_f32_e32 v4, v4, v6
	v_cndmask_b32_e64 v4, v6, v4, s[8:9]
	v_add_f32_e32 v2, v2, v5
	v_add_f32_e32 v5, v5, v4
	v_cndmask_b32_e64 v62, v4, v5, s[10:11]
	v_add_f32_e32 v4, v122, v62
	v_mul_f32_e32 v4, 0x3fb8aa3b, v4
	v_exp_f32_e32 v6, v4
	v_lshlrev_b32_e32 v5, 16, v120
	v_mul_f32_e32 v5, 0x3db504f3, v5
	v_mul_f32_e32 v2, 0x3fb8aa3b, v2
	v_mul_f32_e32 v5, v5, v6
	v_rcp_f32_e32 v4, v6
	v_bfe_u32 v6, v5, 16, 1
	v_add3_u32 v5, v5, v6, s55
	v_lshrrev_b32_e32 v5, 16, v5
	v_lshl_add_u64 v[6:7], s[66:67], 0, v[26:27]
	ds_write_b16 v70, v5 offset:8192
	global_store_short v[6:7], v5, off
	v_add_f32_e32 v5, v123, v62
	v_mul_f32_e32 v5, 0x3fb8aa3b, v5
	v_exp_f32_e32 v5, v5
	v_lshlrev_b32_e32 v6, 16, v119
	v_mul_f32_e32 v7, 0x3db504f3, v6
	v_exp_f32_e32 v2, v2
	v_rcp_f32_e32 v6, v5
	v_mul_f32_e32 v5, v7, v5
	v_bfe_u32 v7, v5, 16, 1
	v_add3_u32 v5, v5, v7, s55
	v_lshrrev_b32_e32 v60, 16, v5
	v_add_f32_e32 v5, v124, v62
	v_mul_f32_e32 v5, 0x3fb8aa3b, v5
	global_store_short v[58:59], v60, off
	v_exp_f32_e32 v58, v5
	v_lshlrev_b32_e32 v7, 16, v117
	v_mul_f32_e32 v7, 0x3db504f3, v7
	v_mul_f32_e32 v7, v7, v58
	v_rcp_f32_e32 v5, v58
	v_bfe_u32 v58, v7, 16, 1
	v_add3_u32 v7, v7, v58, s55
	v_lshrrev_b32_e32 v63, 16, v7
	v_add_f32_e32 v7, v125, v62
	v_lshl_add_u64 v[58:59], s[66:67], 0, v[30:31]
	v_mul_f32_e32 v7, 0x3fb8aa3b, v7
	global_store_short v[58:59], v63, off
	v_exp_f32_e32 v59, v7
	v_lshlrev_b32_e32 v58, 16, v118
	v_mul_f32_e32 v58, 0x3db504f3, v58
	v_mul_f32_e32 v58, v58, v59
	v_rcp_f32_e32 v7, v59
	v_bfe_u32 v59, v58, 16, 1
	v_add3_u32 v58, v58, v59, s55
	v_lshrrev_b32_e32 v64, 16, v58
	v_lshl_add_u64 v[58:59], s[66:67], 0, v[32:33]
	global_store_short v[58:59], v64, off
	v_lshlrev_b32_e32 v59, 16, v114
	v_lshlrev_b32_e32 v58, 16, v115
	v_pk_mul_f32 v[58:59], v[4:5], v[58:59]
	v_lshlrev_b32_e32 v5, 16, v112
	v_bfe_u32 v4, v58, 16, 1
	v_add3_u32 v4, v58, v4, s55
	ds_write_b16_d16_hi v70, v4 offset:25600
	ds_write_b16 v71, v60 offset:8192
	v_lshlrev_b32_e32 v4, 16, v111
	v_pk_mul_f32 v[60:61], v[6:7], v[4:5]
	v_bfe_u32 v6, v59, 16, 1
	v_bfe_u32 v4, v60, 16, 1
	v_add3_u32 v4, v60, v4, s55
	ds_write_b16_d16_hi v71, v4 offset:25600
	v_pk_mul_f32 v[4:5], v[2:3], v[58:59] op_sel_hi:[0,1]
	v_bfe_u32 v58, v61, 16, 1
	v_add3_u32 v58, v61, v58, s55
	ds_write_b16 v72, v63 offset:8192
	ds_write_b16_d16_hi v73, v58 offset:25600
	v_add_f32_e32 v58, v126, v62
	v_add3_u32 v6, v59, v6, s55
	v_mul_f32_e32 v58, 0x3fb8aa3b, v58
	ds_write_b16_d16_hi v72, v6 offset:25600
	v_pk_mul_f32 v[6:7], v[2:3], v[60:61] op_sel_hi:[0,1]
	v_exp_f32_e32 v60, v58
	v_lshlrev_b32_e32 v59, 16, v110
	v_mul_f32_e32 v59, 0x3db504f3, v59
	ds_write_b16 v73, v64 offset:8192
	v_mul_f32_e32 v59, v59, v60
	v_rcp_f32_e32 v58, v60
	v_bfe_u32 v60, v59, 16, 1
	v_add3_u32 v59, v59, v60, s55
	v_lshrrev_b32_e32 v59, 16, v59
	v_lshl_add_u64 v[60:61], s[66:67], 0, v[34:35]
	ds_write_b16 v74, v59 offset:8192
	global_store_short v[60:61], v59, off
	v_add_f32_e32 v59, v127, v62
	v_mul_f32_e32 v59, 0x3fb8aa3b, v59
	v_exp_f32_e32 v59, v59
	v_lshlrev_b32_e32 v60, 16, v109
	v_mul_f32_e32 v61, 0x3db504f3, v60
	v_lshl_add_u64 v[64:65], s[66:67], 0, v[36:37]
	v_rcp_f32_e32 v60, v59
	v_mul_f32_e32 v59, v61, v59
	v_bfe_u32 v61, v59, 16, 1
	v_add3_u32 v59, v59, v61, s55
	v_lshrrev_b32_e32 v63, 16, v59
	v_add_f32_e32 v59, v128, v62
	v_mul_f32_e32 v59, 0x3fb8aa3b, v59
	global_store_short v[64:65], v63, off
	v_exp_f32_e32 v64, v59
	v_lshlrev_b32_e32 v61, 16, v107
	v_mul_f32_e32 v61, 0x3db504f3, v61
	v_mul_f32_e32 v61, v61, v64
	v_rcp_f32_e32 v59, v64
	v_bfe_u32 v64, v61, 16, 1
	v_add3_u32 v61, v61, v64, s55
	v_lshrrev_b32_e32 v107, 16, v61
	v_add_f32_e32 v61, v129, v62
	v_lshl_add_u64 v[64:65], s[66:67], 0, v[38:39]
	v_mul_f32_e32 v61, 0x3fb8aa3b, v61
	global_store_short v[64:65], v107, off
	v_exp_f32_e32 v65, v61
	v_lshlrev_b32_e32 v64, 16, v104
	v_mul_f32_e32 v64, 0x3db504f3, v64
	v_mul_f32_e32 v64, v64, v65
	v_rcp_f32_e32 v61, v65
	v_bfe_u32 v65, v64, 16, 1
	v_add3_u32 v64, v64, v65, s55
	v_lshrrev_b32_e32 v104, 16, v64
	v_lshl_add_u64 v[64:65], s[66:67], 0, v[40:41]
	global_store_short v[64:65], v104, off
	v_lshlrev_b32_e32 v65, 16, v101
	v_lshlrev_b32_e32 v64, 16, v100
	v_pk_mul_f32 v[64:65], v[58:59], v[64:65]
	v_lshlrev_b32_e32 v59, 16, v105
	v_bfe_u32 v58, v64, 16, 1
	v_add3_u32 v58, v64, v58, s55
	ds_write_b16_d16_hi v74, v58 offset:25600
	ds_write_b16 v75, v63 offset:8192
	v_lshlrev_b32_e32 v58, 16, v102
	v_pk_mul_f32 v[66:67], v[60:61], v[58:59]
	v_bfe_u32 v60, v65, 16, 1
	v_bfe_u32 v58, v66, 16, 1
	v_bfe_u32 v63, v67, 16, 1
	v_add3_u32 v58, v66, v58, s55
	v_add3_u32 v60, v65, v60, s55
	v_add3_u32 v63, v67, v63, s55
	ds_write_b16_d16_hi v75, v58 offset:25600
	ds_write_b16 v76, v107 offset:8192
	ds_write_b16_d16_hi v76, v60 offset:25600
	ds_write_b16_d16_hi v77, v63 offset:25600
	v_add_f32_e32 v63, v132, v62
	v_mul_f32_e32 v63, 0x3fb8aa3b, v63
	v_exp_f32_e32 v63, v63
	v_pk_mul_f32 v[58:59], v[2:3], v[64:65] op_sel_hi:[0,1]
	v_lshlrev_b32_e32 v64, 16, v116
	v_mul_f32_e32 v65, 0x3db504f3, v64
	v_rcp_f32_e32 v64, v63
	v_mul_f32_e32 v63, v65, v63
	v_bfe_u32 v65, v63, 16, 1
	v_add3_u32 v63, v63, v65, s55
	v_pk_mul_f32 v[60:61], v[2:3], v[66:67] op_sel_hi:[0,1]
	v_lshrrev_b32_e32 v63, 16, v63
	v_lshl_add_u64 v[66:67], s[66:67], 0, v[42:43]
	ds_write_b16 v77, v104 offset:8192
; __device__ __forceinline__ unsigned f2bf(float f) { unsigned u = __builtin_bit_cast(unsigned, f); return (u + 0x7fffu + ((u >> 16) & 1u)) >> 16; }
; __device__ __forceinline__ unsigned pk2(float lo, float hi) { return f2bf(lo) | (f2bf(hi) << 16); }
; __device__ __forceinline__ void gla_prep_unit(Frame& F, int unit) {
;     ...
;     for (int i = 0; i < 16; i += 2) { float kdv[2];
; #pragma unroll
;         for (int u = 0; u < 2; ++u) { const int c = cg * 16 + i + u; const float bb = bl[i + u] + offs;
;             const float q = bf2f(qv[i + u]) * 0.08838834764831845f, k = bf2f(kv[i + u]);
;             const float eb = __expf(bb), einv = __builtin_amdgcn_rcpf(eb);
;             const float qin = q * eb, kin = k * einv; kdv[u] = kin * eblast;
;             const bf16_t qb16 = (bf16_t)f2bf(qin); qinS[c * GP_ROW + d] = qb16; kinS[c * GP_ROW + d] = (bf16_t)f2bf(kin); QIN[c * 128 + d] = qb16; }
;         kd[i >> 1] = pk2(kdv[0], kdv[1]); }
;     *(u32x4*)(KDT + d * 64 + cg * 16) = (u32x4){kd[0], kd[1], kd[2], kd[3]}; *(u32x4*)(KDT + d * 64 + cg * 16 + 8) = (u32x4){kd[4], kd[5], kd[6], kd[7]};
;     if (cg == 0) DEC[d] = eblast;
	ds_write_b16 v78, v63 offset:8192
	global_store_short v[66:67], v63, off
	v_add_f32_e32 v63, v133, v62
	v_mul_f32_e32 v63, 0x3fb8aa3b, v63
	v_exp_f32_e32 v63, v63
	v_lshlrev_b32_e32 v65, 16, v113
	v_mul_f32_e32 v65, 0x3db504f3, v65
	v_lshl_add_u64 v[100:101], s[66:67], 0, v[44:45]
	v_rcp_f32_e32 v66, v63
	v_mul_f32_e32 v63, v65, v63
	v_bfe_u32 v65, v63, 16, 1
	v_add3_u32 v63, v63, v65, s55
	v_add_f32_e32 v65, v134, v62
	v_lshrrev_b32_e32 v63, 16, v63
	v_mul_f32_e32 v65, 0x3fb8aa3b, v65
	global_store_short v[100:101], v63, off
	v_exp_f32_e32 v100, v65
	v_lshlrev_b32_e32 v67, 16, v108
	v_mul_f32_e32 v67, 0x3db504f3, v67
	v_mul_f32_e32 v67, v67, v100
	v_rcp_f32_e32 v65, v100
	v_bfe_u32 v100, v67, 16, 1
	v_add3_u32 v67, v67, v100, s55
	v_lshrrev_b32_e32 v102, 16, v67
	v_add_f32_e32 v67, v135, v62
	v_lshl_add_u64 v[100:101], s[66:67], 0, v[46:47]
	v_mul_f32_e32 v67, 0x3fb8aa3b, v67
	global_store_short v[100:101], v102, off
	v_exp_f32_e32 v101, v67
	v_lshlrev_b32_e32 v100, 16, v106
	v_mul_f32_e32 v100, 0x3db504f3, v100
	v_mul_f32_e32 v100, v100, v101
	v_rcp_f32_e32 v67, v101
	v_bfe_u32 v101, v100, 16, 1
	v_add3_u32 v100, v100, v101, s55
	v_lshrrev_b32_e32 v104, 16, v100
	v_lshl_add_u64 v[100:101], s[66:67], 0, v[48:49]
	global_store_short v[100:101], v104, off
	v_lshlrev_b32_e32 v101, 16, v103
	v_lshlrev_b32_e32 v100, 16, v99
	v_pk_mul_f32 v[64:65], v[64:65], v[100:101]
	v_lshl_add_u64 v[100:101], s[66:67], 0, v[52:53]
	v_bfe_u32 v99, v64, 16, 1
	v_add3_u32 v99, v64, v99, s55
	ds_write_b16_d16_hi v78, v99 offset:25600
	ds_write_b16 v79, v63 offset:8192
	v_lshlrev_b32_e32 v99, 16, v98
	v_lshlrev_b32_e32 v98, 16, v97
	v_pk_mul_f32 v[66:67], v[66:67], v[98:99]
	v_pk_mul_f32 v[98:99], v[2:3], v[64:65] op_sel_hi:[0,1]
	v_bfe_u32 v63, v66, 16, 1
	v_add3_u32 v63, v66, v63, s55
	ds_write_b16_d16_hi v79, v63 offset:25600
	v_bfe_u32 v63, v65, 16, 1
	v_add3_u32 v63, v65, v63, s55
	ds_write_b16_d16_hi v80, v63 offset:25600
	v_bfe_u32 v63, v67, 16, 1
	v_add3_u32 v63, v67, v63, s55
	ds_write_b16 v80, v102 offset:8192
	ds_write_b16_d16_hi v81, v63 offset:25600
	v_add_f32_e32 v63, v136, v62
	v_mul_f32_e32 v63, 0x3fb8aa3b, v63
	v_exp_f32_e32 v63, v63
	v_pk_mul_f32 v[64:65], v[2:3], v[66:67] op_sel_hi:[0,1]
	v_lshlrev_b32_e32 v66, 16, v96
	v_mul_f32_e32 v67, 0x3db504f3, v66
	v_rcp_f32_e32 v66, v63
	v_mul_f32_e32 v63, v67, v63
	v_bfe_u32 v67, v63, 16, 1
	v_add3_u32 v63, v63, v67, s55
	v_lshrrev_b32_e32 v63, 16, v63
	v_lshl_add_u64 v[96:97], s[66:67], 0, v[50:51]
	ds_write_b16 v81, v104 offset:8192
	ds_write_b16 v82, v63 offset:8192
	global_store_short v[96:97], v63, off
	v_add_f32_e32 v63, v137, v62
	v_mul_f32_e32 v63, 0x3fb8aa3b, v63
	v_exp_f32_e32 v63, v63
	v_lshlrev_b32_e32 v67, 16, v95
	v_mul_f32_e32 v67, 0x3db504f3, v67
	v_add_f32_e32 v3, v62, v3
	v_rcp_f32_e32 v96, v63
	v_mul_f32_e32 v63, v67, v63
	v_bfe_u32 v67, v63, 16, 1
	v_add3_u32 v63, v63, v67, s55
	v_lshrrev_b32_e32 v102, 16, v63
	v_add_f32_e32 v63, v138, v62
	v_mul_f32_e32 v63, 0x3fb8aa3b, v63
	v_mul_f32_e32 v3, 0x3fb8aa3b, v3
	v_exp_f32_e32 v63, v63
	v_exp_f32_e32 v3, v3
	v_lshlrev_b32_e32 v67, 16, v94
	v_lshlrev_b32_e32 v62, 16, v93
	v_mul_f32_e32 v94, 0x3db504f3, v67
	v_mul_f32_e32 v62, 0x3db504f3, v62
	v_rcp_f32_e32 v67, v63
	v_mul_f32_e32 v63, v94, v63
	v_rcp_f32_e32 v97, v3
	v_mul_f32_e32 v3, v62, v3
	v_bfe_u32 v94, v63, 16, 1
	v_bfe_u32 v62, v3, 16, 1
	v_add3_u32 v63, v63, v94, s55
	v_add3_u32 v3, v3, v62, s55
	global_store_short v[100:101], v102, off
	v_lshrrev_b32_e32 v100, 16, v63
	v_lshl_add_u64 v[94:95], s[66:67], 0, v[54:55]
	v_lshrrev_b32_e32 v3, 16, v3
	v_lshl_add_u64 v[62:63], s[66:67], 0, v[56:57]
	global_store_short v[94:95], v100, off
	global_store_short v[62:63], v3, off
	v_lshlrev_b32_e32 v63, 16, v92
	v_lshlrev_b32_e32 v62, 16, v91
	v_pk_mul_f32 v[62:63], v[66:67], v[62:63]
	v_lshlrev_b32_e32 v67, 16, v90
	v_bfe_u32 v66, v62, 16, 1
	v_add3_u32 v66, v62, v66, s55
	ds_write_b16_d16_hi v82, v66 offset:25600
	ds_write_b16 v83, v102 offset:8192
	v_lshlrev_b32_e32 v66, 16, v89
	v_pk_mul_f32 v[66:67], v[96:97], v[66:67]
	v_pk_mul_f32 v[90:91], v[2:3], v[62:63] op_sel_hi:[0,1]
	v_bfe_u32 v89, v66, 16, 1
	v_bfe_u32 v62, v63, 16, 1
	v_add3_u32 v89, v66, v89, s55
	v_add3_u32 v62, v63, v62, s55
	ds_write_b16_d16_hi v83, v89 offset:25600
	ds_write_b16 v84, v100 offset:8192
	ds_write_b16_d16_hi v84, v62 offset:25600
	v_pk_mul_f32 v[62:63], v[2:3], v[66:67] op_sel_hi:[0,1]
	ds_write_b16 v85, v3 offset:8192
	v_bfe_u32 v3, v67, 16, 1
	v_add3_u32 v3, v67, v3, s55
	v_bfe_u32 v67, v7, 16, 1
	v_bfe_u32 v66, v60, 16, 1
	v_bfe_u32 v89, v6, 16, 1
	v_add3_u32 v67, v7, v67, s55
	v_bfe_u32 v7, v58, 16, 1
	ds_write_b16_d16_hi v85, v3 offset:25600
	v_bfe_u32 v3, v61, 16, 1
	v_add3_u32 v89, v6, v89, s55
	v_add3_u32 v6, v60, v66, s55
	v_bfe_u32 v60, v59, 16, 1
	v_add3_u32 v7, v58, v7, s55
	v_add3_u32 v3, v61, v3, s55
	v_bfe_u32 v61, v4, 16, 1
	v_bfe_u32 v66, v5, 16, 1
	v_add3_u32 v59, v59, v60, s55
	v_lshrrev_b32_e32 v58, 16, v7
	v_add3_u32 v5, v5, v66, s55
	v_add3_u32 v4, v4, v61, s55
	v_lshrrev_b32_e32 v7, 16, v59
	v_and_or_b32 v6, v6, s45, v58
	v_lshl_add_u64 v[58:59], s[66:67], 0, v[24:25]
	v_lshrrev_b32_e32 v4, 16, v4
	v_lshrrev_b32_e32 v5, 16, v5
	v_add_co_u32_e32 v58, vcc, s56, v58
	v_and_or_b32 v7, v3, s45, v7
	v_and_or_b32 v5, v67, s45, v5
	v_and_or_b32 v4, v89, s45, v4
	v_addc_co_u32_e32 v59, vcc, 0, v59, vcc
	global_store_dwordx4 v[58:59], v[4:7], off
	v_bfe_u32 v61, v90, 16, 1
	v_bfe_u32 v3, v63, 16, 1
	v_bfe_u32 v4, v62, 16, 1
	v_bfe_u32 v6, v64, 16, 1
	v_add3_u32 v60, v64, v6, s55
	v_add3_u32 v4, v62, v4, s55
	v_bfe_u32 v6, v98, 16, 1
	v_bfe_u32 v7, v99, 16, 1
	v_bfe_u32 v62, v91, 16, 1
	v_bfe_u32 v5, v65, 16, 1
	v_add3_u32 v62, v91, v62, s55
	v_add3_u32 v61, v90, v61, s55
	v_add3_u32 v7, v99, v7, s55
	v_add3_u32 v6, v98, v6, s55
	v_add3_u32 v5, v65, v5, s55
	v_add3_u32 v3, v63, v3, s55
	v_lshrrev_b32_e32 v63, 16, v6
	v_lshrrev_b32_e32 v64, 16, v7
	v_lshrrev_b32_e32 v6, 16, v61
	v_lshrrev_b32_e32 v7, 16, v62
	v_and_or_b32 v7, v3, s45, v7
	v_and_or_b32 v6, v4, s45, v6
	v_and_or_b32 v5, v5, s45, v64
	v_and_or_b32 v4, v60, s45, v63
	global_store_dwordx4 v[58:59], v[4:7], off offset:16
	s_and_saveexec_b64 s[0:1], s[4:5]
	s_cbranch_execz .LBB0_266
	v_readlane_b32 s60, v254, 25
	v_readlane_b32 s66, v254, 31
	v_readlane_b32 s67, v254, 32
	v_readlane_b32 s61, v254, 26
	v_readlane_b32 s62, v254, 27
	v_lshl_add_u64 v[4:5], s[66:67], 0, v[18:19]
	v_readlane_b32 s63, v254, 28
	v_readlane_b32 s64, v254, 29
	v_readlane_b32 s65, v254, 30
	global_store_dword v[4:5], v2, off

; #define LAS __attribute__((address_space(3)))
; __device__ __forceinline__ void swa_unit(Frame& F, int b, int kvh, int qb) {
;     ...
;     const int tid = F.tid, lane = F.lane, r32 = lane & 31, hi = lane >> 5;
;     const int K0 = 64 * (qb - 2);
;     const size_t rowb = (size_t)b * SEQ;
;     for (int task = tid; task < 768; task += NTHREADS) { const int key = task >> 2, c = task & 3, kg = K0 + key;
;         u32x4 o1 = (u32x4){0u, 0u, 0u, 0u}, o2 = o1;
;         if (kg >= 0) { const bf16_t* src = PROJ + (rowb + kg) * LDP + C_SK + kvh * 64; const u32x4 x1 = *(const u32x4*)(src + 8 * c), x2 = *(const u32x4*)(src + 32 + 8 * c);
;             const float* cs = RC + (rowb + kg) * 32 + 8 * c; const float* sn = RS + (rowb + kg) * 32 + 8 * c;
;             rot8(x1, x2, *(const f32x4*)cs, *(const f32x4*)(cs + 4), *(const f32x4*)sn, *(const f32x4*)(sn + 4), 1.0f, o1, o2); }
;         *(LAS u32x4*)(Kl + key * SWA_KROW + 16 * c) = o1; *(LAS u32x4*)(Kl + key * SWA_KROW + 64 + 16 * c) = o2; }
;     for (int task = tid; task < 1536; task += NTHREADS) { const int key = task >> 3, c = task & 7, kg = K0 + key;
;         u32x4 v = (u32x4){0u, 0u, 0u, 0u};
;         if (kg >= 0) v = *(const u32x4*)(PROJ + (rowb + kg) * LDP + C_SV + kvh * 64 + 8 * c);
;         *(LAS u32x4*)(Vl + key * SWA_KROW + 16 * c) = v; }
;     __syncthreads();
;     const int qh = kvh * 8 + F.wave;
;     const float sink2 = F.sinks[qh] * 1.4426950408889634f;
.LBB0_273:
	s_ashr_i32 s44, s89, 9
	s_and_b32 s0, s88, 0x7f
	s_bfe_u32 s4, s89, 0x20007
	s_ashr_i32 s45, s44, 31
	s_lshl_b32 s10, s0, 6
	s_lshl_b64 s[90:91], s[44:45], 13
	s_lshl_b32 s5, s4, 6
	s_lshl_b32 s98, s4, 3
	v_readlane_b32 s99, v254, 23
	s_add_i32 s98, s98, s99
	s_lshl_b32 s98, s98, 2
	v_mov_b32_e32 v192, s98
	global_load_dword v192, v192, s[78:79]
	v_add_u32_e32 v6, s10, v114
	v_mov_b32_e32 v7, v83
	v_add_u32_e32 v172, 64, v6
	v_mov_b32_e32 v173, v83
	v_add_u32_e32 v174, 0x80, v6
	v_mov_b32_e32 v175, v83
	v_mov_b32_e32 v101, v83
	s_lshl_b32 s0, s5, 1
	v_cmp_lt_i32_e32 vcc, -1, v6
	v_mov_b32_e32 v176, 0
	v_mov_b32_e32 v177, 0
	v_mov_b32_e32 v178, 0
	v_mov_b32_e32 v179, 0
	s_and_saveexec_b64 s[46:47], vcc
	v_lshl_add_u64 v[188:189], s[90:91], 0, v[6:7]
	v_mov_b64_e32 v[190:191], s[96:97]
	v_mad_u64_u32 v[190:191], s[50:51], v188, s85, v[190:191]
	v_mad_i32_i24 v191, v189, s85, v191
	v_lshl_add_u64 v[188:189], v[190:191], 0, s[0:1]
	v_lshl_add_u64 v[188:189], v[188:189], 0, v[100:101]
	v_add_co_u32_e32 v188, vcc, 0x4000, v188
	s_nop 1
	v_addc_co_u32_e32 v189, vcc, 0, v189, vcc
	global_load_dwordx4 v[176:179], v[188:189], off offset:512
	s_or_b64 exec, exec, s[46:47]
	v_cmp_lt_i32_e32 vcc, -1, v172
	v_mov_b32_e32 v180, 0
	v_mov_b32_e32 v181, 0
	v_mov_b32_e32 v182, 0
	v_mov_b32_e32 v183, 0
	s_and_saveexec_b64 s[46:47], vcc
	v_lshl_add_u64 v[188:189], s[90:91], 0, v[172:173]
	v_mov_b64_e32 v[190:191], s[96:97]
	v_mad_u64_u32 v[190:191], s[50:51], v188, s85, v[190:191]
	v_mad_i32_i24 v191, v189, s85, v191
	v_lshl_add_u64 v[188:189], v[190:191], 0, s[0:1]
	v_lshl_add_u64 v[188:189], v[188:189], 0, v[100:101]
	v_add_co_u32_e32 v188, vcc, 0x4000, v188
	s_nop 1
	v_addc_co_u32_e32 v189, vcc, 0, v189, vcc
	global_load_dwordx4 v[180:183], v[188:189], off offset:512
	s_or_b64 exec, exec, s[46:47]
	v_cmp_lt_i32_e32 vcc, -1, v174
	v_mov_b32_e32 v184, 0
	v_mov_b32_e32 v185, 0
	v_mov_b32_e32 v186, 0
	v_mov_b32_e32 v187, 0
	s_and_saveexec_b64 s[46:47], vcc
	v_lshl_add_u64 v[188:189], s[90:91], 0, v[174:175]
	v_mov_b64_e32 v[190:191], s[96:97]
	v_mad_u64_u32 v[190:191], s[50:51], v188, s85, v[190:191]
	v_mad_i32_i24 v191, v189, s85, v191
	v_lshl_add_u64 v[188:189], v[190:191], 0, s[0:1]
	v_lshl_add_u64 v[188:189], v[188:189], 0, v[100:101]
	v_add_co_u32_e32 v188, vcc, 0x4000, v188
	s_nop 1
	v_addc_co_u32_e32 v189, vcc, 0, v189, vcc
	global_load_dwordx4 v[184:187], v[188:189], off offset:512
	s_or_b64 exec, exec, s[46:47]
	s_mov_b64 s[44:45], exec
	v_readlane_b32 s46, v254, 56
	v_readlane_b32 s47, v254, 57
	s_and_b64 s[46:47], s[44:45], s[46:47]
	s_mov_b64 exec, s[46:47]
	s_cbranch_execz .LBB0_278
	v_add_u32_e32 v10, s10, v111
	s_mov_b64 s[46:47], 0
	v_mov_b32_e32 v12, v113
	v_mov_b32_e32 v13, v112
	s_branch .LBB0_276

; #define LAS __attribute__((address_space(3)))
; __device__ __forceinline__ void swa_unit(Frame& F, int b, int kvh, int qb) {
;     ...
;     for (int task = tid; task < 1536; task += NTHREADS) { const int key = task >> 3, c = task & 7, kg = K0 + key;
;         u32x4 v = (u32x4){0u, 0u, 0u, 0u};
;         if (kg >= 0) v = *(const u32x4*)(PROJ + (rowb + kg) * LDP + C_SV + kvh * 64 + 8 * c);
;         *(LAS u32x4*)(Vl + key * SWA_KROW + 16 * c) = v; }
;     __syncthreads();
;     const int qh = kvh * 8 + F.wave;
;     const float sink2 = F.sinks[qh] * 1.4426950408889634f;
.LBB0_278:
	s_or_b64 exec, exec, s[44:45]
	s_waitcnt vmcnt(0)
	ds_write_b128 v115, v[176:179]
	ds_write_b128 v115, v[180:183] offset:9216
	ds_write_b128 v115, v[184:187] offset:18432
.LBB0_282:
	s_lshl_b32 s0, s4, 3
	v_readlane_b32 s4, v254, 23
	s_add_i32 s0, s0, s4
	s_lshl_b32 s4, s0, 2
	v_mov_b32_e32 v2, s4
	s_waitcnt lgkmcnt(0)
	s_barrier
	s_and_b32 s10, s89, 0x7f
	v_readlane_b32 s5, v254, 24
	s_lshl_b32 s84, s10, 6
	s_add_i32 s4, s84, 0xffffff80
	s_lshl_b32 s5, s0, 6
	s_cmp_gt_u32 s10, 1
	v_readlane_b32 s46, v254, 58
	s_cselect_b64 s[74:75], -1, 0
	v_readlane_b32 s47, v254, 59
	s_mov_b32 s11, 0
	s_and_b64 s[44:45], s[74:75], s[8:9]
	s_and_b64 s[46:47], s[74:75], s[46:47]
	s_and_b64 s[48:49], s[74:75], s[12:13]
	s_and_b64 s[50:51], s[74:75], s[14:15]
	s_and_b64 s[52:53], s[74:75], s[16:17]
	s_and_b64 s[54:55], s[74:75], s[18:19]
	s_and_b64 s[56:57], s[74:75], s[20:21]
	s_and_b64 s[58:59], s[74:75], s[22:23]
	s_and_b64 s[60:61], s[74:75], s[24:25]
	s_and_b64 s[62:63], s[74:75], s[26:27]
	s_and_b64 s[64:65], s[74:75], s[28:29]
	s_and_b64 s[66:67], s[74:75], s[30:31]
	s_and_b64 s[68:69], s[74:75], s[34:35]
	s_and_b64 s[70:71], s[74:75], s[36:37]
	s_and_b64 s[72:73], s[74:75], s[38:39]
	s_and_b64 s[74:75], s[74:75], s[40:41]
	s_mov_b64 s[94:95], -1
	v_mov_b32_e32 v2, v192
	v_mul_f32_e32 v99, 0x3fb8aa3b, v192
	s_branch .LBB0_284
